# al1_aligned
# speedup vs baseline: 1.0097x; 1.0026x over previous
.LBB1_12:
	v_sub_f32_e32 v2, v2, v242
	v_exp_f32_e32 v64, v2
	v_sub_f32_e32 v2, v19, v242
	v_exp_f32_e32 v81, v2
	v_sub_f32_e32 v2, v3, v242
	v_exp_f32_e32 v65, v2
	v_sub_f32_e32 v2, v20, v242
	v_exp_f32_e32 v82, v2
	v_sub_f32_e32 v2, v4, v242
	v_exp_f32_e32 v66, v2
	v_sub_f32_e32 v2, v21, v242
	v_exp_f32_e32 v83, v2
	v_sub_f32_e32 v2, v5, v242
	v_exp_f32_e32 v67, v2
	v_sub_f32_e32 v2, v22, v242
	v_exp_f32_e32 v84, v2
	v_sub_f32_e32 v2, v6, v242
	v_exp_f32_e32 v68, v2
	v_sub_f32_e32 v2, v23, v242
	v_exp_f32_e32 v85, v2
	v_sub_f32_e32 v2, v7, v242
	v_exp_f32_e32 v69, v2
	v_sub_f32_e32 v2, v24, v242
	v_exp_f32_e32 v86, v2
	v_sub_f32_e32 v2, v8, v242
	v_exp_f32_e32 v70, v2
	v_sub_f32_e32 v2, v25, v242
	v_exp_f32_e32 v87, v2
	v_sub_f32_e32 v2, v9, v242
	v_exp_f32_e32 v71, v2
	v_sub_f32_e32 v2, v26, v242
	v_exp_f32_e32 v88, v2
	v_sub_f32_e32 v2, v10, v242
	v_exp_f32_e32 v72, v2
	v_sub_f32_e32 v2, v27, v242
	v_exp_f32_e32 v89, v2
	v_sub_f32_e32 v2, v11, v242
	v_exp_f32_e32 v73, v2
	v_sub_f32_e32 v2, v28, v242
	v_exp_f32_e32 v90, v2
	v_sub_f32_e32 v2, v12, v242
	v_exp_f32_e32 v74, v2
	v_sub_f32_e32 v2, v29, v242
	v_exp_f32_e32 v91, v2
	v_sub_f32_e32 v2, v13, v242
	v_exp_f32_e32 v75, v2
	v_sub_f32_e32 v2, v30, v242
	v_exp_f32_e32 v92, v2
	v_sub_f32_e32 v2, v14, v242
	v_exp_f32_e32 v76, v2
	v_sub_f32_e32 v2, v31, v242
	v_exp_f32_e32 v93, v2
	v_sub_f32_e32 v2, v15, v242
	v_exp_f32_e32 v77, v2
	v_sub_f32_e32 v2, v32, v242
	v_exp_f32_e32 v94, v2
	v_sub_f32_e32 v2, v16, v242
	v_exp_f32_e32 v78, v2
	v_sub_f32_e32 v2, v33, v242
	v_sub_f32_e32 v18, v18, v242
	v_exp_f32_e32 v95, v2
	v_sub_f32_e32 v2, v17, v242
	v_exp_f32_e32 v80, v18
	v_exp_f32_e32 v79, v2
	s_add_i32 s0, s43, 0x80
	s_and_b32 s1, s3, 0x3fffffc0
	v_lshlrev_b32_e32 v2, 1, v0
	v_and_b32_e32 v2, 32, v2
	v_lshlrev_b32_e32 v4, 4, v0
	s_lshr_b32 s40, s0, 6
	s_lshl_b32 s0, s1, 2
	s_lshl_b32 s36, s19, 6
	v_add3_u32 v2, 0, v2, v38
	v_lshlrev_b32_e32 v3, 8, v212
	s_add_i32 s37, s0, 0
	v_and_b32_e32 v4, 0xc0, v4
	s_mov_b32 s14, 1
	v_add3_u32 v240, v2, v3, v4
	s_cmp_lt_u32 s18, 2
	v_add_u32_e32 v202, s4, v1
	v_and_b32_e32 v213, 3, v0
	s_cbranch_scc1 .LBB1_28
	s_lshl_b32 s5, s2, 4
	s_lshl_b32 s4, s42, 7
	s_and_b32 s5, s5, 0x400
	s_lshl_b32 s14, s2, 15
	s_lshr_b32 s16, s3, 2
	s_or_b32 s4, s5, s4
	s_and_b32 s14, s14, 0x400000
	v_mov_b32_e32 v201, 0
	s_and_b32 s16, s16, 0x3ffffff0
	s_mov_b32 s5, 0
	s_add_u32 s16, s6, s16
	v_mov_b32_e32 v203, v201
	s_mov_b32 s15, s5
	s_addc_u32 s17, s7, 0
	v_lshlrev_b64 v[0:1], 11, v[202:203]
	s_add_u32 s16, s16, s14
	v_lshl_add_u64 v[0:1], s[14:15], 0, v[0:1]
	v_lshlrev_b32_e32 v16, 4, v212
	s_addc_u32 s17, s17, 0
	v_lshl_or_b32 v0, v213, 4, v0
	v_mov_b32_e32 v14, v201
	v_mov_b32_e32 v15, v201
	v_lshl_add_u64 v[204:205], s[16:17], 0, v[200:201]
	v_lshl_add_u64 v[206:207], s[8:9], 0, v[0:1]
	s_add_u32 s52, s16, s4
	s_addc_u32 s53, s17, 0
	s_add_u32 s54, s8, s14
	s_addc_u32 s55, s9, s15
	s_add_u32 s54, s54, s4
	s_addc_u32 s55, s55, 0
	v_lshlrev_b32_e32 v250, 11, v202
	v_lshl_or_b32 v250, v213, 4, v250
	v_mov_b32_e32 v0, v201
	v_mov_b32_e32 v1, v201
	v_mov_b32_e32 v2, v201
	v_mov_b32_e32 v3, v201
	v_mov_b32_e32 v4, v201
	v_mov_b32_e32 v5, v201
	v_mov_b32_e32 v6, v201
	v_mov_b32_e32 v7, v201
	v_mov_b32_e32 v8, v201
	v_mov_b32_e32 v9, v201
	v_mov_b32_e32 v10, v201
	v_mov_b32_e32 v11, v201
	v_mov_b32_e32 v12, v201
	v_mov_b32_e32 v13, v201
	v_add_u32_e32 v201, s37, v16
	v_mov_b64_e32 v[30:31], v[14:15]
	v_mov_b64_e32 v[46:47], v[14:15]
	v_cmp_gt_u32_e64 s[0:1], 32, v236
	v_lshl_add_u32 v214, v238, 2, s37
	s_movk_i32 s45, 0x4000
	s_movk_i32 s48, 0x2000
	s_mov_b32 s46, 5
	s_mov_b64 s[14:15], 0x80000
	s_mov_b64 s[16:17], 0x80040
	s_mov_b64 s[18:19], 0x40000
	s_mov_b64 s[20:21], 0x40040
	s_mov_b32 s47, 0x41000000
	s_mov_b64 s[22:23], 0xa0000
	s_mov_b64 s[24:25], 0xa0040
	s_mov_b64 s[26:27], 0x60000
	s_mov_b64 s[28:29], 0x60040
	v_mov_b64_e32 v[28:29], v[12:13]
	v_mov_b64_e32 v[26:27], v[10:11]
	v_mov_b64_e32 v[24:25], v[8:9]
	v_mov_b64_e32 v[22:23], v[6:7]
	v_mov_b64_e32 v[20:21], v[4:5]
	v_mov_b64_e32 v[18:19], v[2:3]
	v_mov_b64_e32 v[16:17], v[0:1]
	v_mov_b64_e32 v[44:45], v[12:13]
	v_mov_b64_e32 v[42:43], v[10:11]
	v_mov_b64_e32 v[40:41], v[8:9]
	v_mov_b64_e32 v[38:39], v[6:7]
	v_mov_b64_e32 v[36:37], v[4:5]
	v_mov_b64_e32 v[34:35], v[2:3]
	v_mov_b64_e32 v[32:33], v[0:1]
	s_mov_b32 s30, s5
	.p2align	6

.LBB2_3:
	s_load_dwordx8 s[12:19], s[0:1], 0x10
	v_lshrrev_b32_e32 v2, 2, v0
	s_lshr_b32 s5, s21, 8
	v_sub_u32_e32 v2, 0, v2
	v_and_b32_e32 v102, 15, v0
	v_bitop3_b32 v2, v120, v2, 3 bitop3:0x78
	s_mul_i32 s25, s5, 0x60
	s_and_b32 s2, s22, 3
	v_lshlrev_b32_e32 v98, 4, v2
	v_or_b32_e32 v2, s25, v102
	v_mov_b32_e32 v50, 0
	s_mov_b32 s3, 0
	v_lshlrev_b32_e32 v99, 6, v2
	s_lshl_b32 s6, s2, 12
	s_mov_b32 s7, 32
	v_mov_b32_e32 v51, v50
	v_mov_b32_e32 v52, v50
	v_mov_b32_e32 v53, v50
	v_mov_b32_e32 v74, v50
	v_mov_b32_e32 v75, v50
	v_mov_b32_e32 v76, v50
	v_mov_b32_e32 v77, v50
	v_mov_b32_e32 v6, v50
	v_mov_b32_e32 v7, v50
	v_mov_b32_e32 v8, v50
	v_mov_b32_e32 v9, v50
	v_mov_b32_e32 v26, v50
	v_mov_b32_e32 v27, v50
	v_mov_b32_e32 v28, v50
	v_mov_b32_e32 v29, v50
	v_mov_b32_e32 v54, v50
	v_mov_b32_e32 v55, v50
	v_mov_b32_e32 v56, v50
	v_mov_b32_e32 v57, v50
	v_mov_b32_e32 v86, v50
	v_mov_b32_e32 v87, v50
	v_mov_b32_e32 v88, v50
	v_mov_b32_e32 v89, v50
	v_mov_b32_e32 v18, v50
	v_mov_b32_e32 v19, v50
	v_mov_b32_e32 v20, v50
	v_mov_b32_e32 v21, v50
	v_mov_b32_e32 v42, v50
	v_mov_b32_e32 v43, v50
	v_mov_b32_e32 v44, v50
	v_mov_b32_e32 v45, v50
	v_mov_b32_e32 v66, v50
	v_mov_b32_e32 v67, v50
	v_mov_b32_e32 v68, v50
	v_mov_b32_e32 v69, v50
	v_mov_b32_e32 v90, v50
	v_mov_b32_e32 v91, v50
	v_mov_b32_e32 v92, v50
	v_mov_b32_e32 v93, v50
	v_mov_b32_e32 v22, v50
	v_mov_b32_e32 v23, v50
	v_mov_b32_e32 v24, v50
	v_mov_b32_e32 v25, v50
	v_mov_b32_e32 v46, v50
	v_mov_b32_e32 v47, v50
	v_mov_b32_e32 v48, v50
	v_mov_b32_e32 v49, v50
	v_mov_b32_e32 v70, v50
	v_mov_b32_e32 v71, v50
	v_mov_b32_e32 v72, v50
	v_mov_b32_e32 v73, v50
	v_mov_b32_e32 v94, v50
	v_mov_b32_e32 v95, v50
	v_mov_b32_e32 v96, v50
	v_mov_b32_e32 v97, v50
	v_mov_b32_e32 v38, v50
	v_mov_b32_e32 v39, v50
	v_mov_b32_e32 v40, v50
	v_mov_b32_e32 v41, v50
	v_mov_b32_e32 v14, v50
	v_mov_b32_e32 v15, v50
	v_mov_b32_e32 v16, v50
	v_mov_b32_e32 v17, v50
	v_mov_b32_e32 v82, v50
	v_mov_b32_e32 v83, v50
	v_mov_b32_e32 v84, v50
	v_mov_b32_e32 v85, v50
	v_mov_b32_e32 v58, v50
	v_mov_b32_e32 v59, v50
	v_mov_b32_e32 v60, v50
	v_mov_b32_e32 v61, v50
	v_mov_b32_e32 v30, v50
	v_mov_b32_e32 v31, v50
	v_mov_b32_e32 v32, v50
	v_mov_b32_e32 v33, v50
	v_mov_b32_e32 v10, v50
	v_mov_b32_e32 v11, v50
	v_mov_b32_e32 v12, v50
	v_mov_b32_e32 v13, v50
	v_mov_b32_e32 v78, v50
	v_mov_b32_e32 v79, v50
	v_mov_b32_e32 v80, v50
	v_mov_b32_e32 v81, v50
	v_mov_b32_e32 v62, v50
	v_mov_b32_e32 v63, v50
	v_mov_b32_e32 v64, v50
	v_mov_b32_e32 v65, v50
	v_mov_b32_e32 v34, v50
	v_mov_b32_e32 v35, v50
	v_mov_b32_e32 v36, v50
	v_mov_b32_e32 v37, v50
	v_mov_b32_e32 v2, v50
	v_mov_b32_e32 v3, v50
	v_mov_b32_e32 v4, v50
	v_mov_b32_e32 v5, v50
	v_lshlrev_b32_e32 v100, 6, v102
	v_add_u32_e32 v99, v99, v98
	v_add3_u32 v100, s6, v100, v98
	s_barrier
	ds_read_b128 v[104:107], v100 offset:12288
	ds_read_b128 v[108:111], v100 offset:13312
	ds_read_b128 v[112:115], v100 offset:14336
	ds_read_b128 v[116:119], v100 offset:15360
	ds_read_b128 v[122:125], v99
	ds_read_b128 v[126:129], v99 offset:1024
	ds_read_b128 v[130:133], v99 offset:2048
	ds_read_b128 v[134:137], v99 offset:3072
	ds_read_b128 v[138:141], v99 offset:4096
	ds_read_b128 v[142:145], v99 offset:5120
	s_mov_b32 s3, 1
	s_mov_b32 s7, 16
	.p2align	6

.LBB2_6:
	s_load_dwordx4 s[0:3], s[0:1], 0x0
	s_add_i32 s9, s22, -8
	s_mov_b32 s28, s23
	s_mov_b32 s29, s20
	v_and_b32_e32 v1, 63, v0
	v_bfe_u32 v3, v0, 4, 2
	v_lshrrev_b32_e32 v2, 2, v1
	v_sub_u32_e32 v3, 0, v3
	v_and_b32_e32 v3, 3, v3
	v_and_b32_e32 v4, 3, v1
	v_xor_b32_e32 v3, v3, v4
	v_lshlrev_b32_e32 v3, 4, v3
	v_lshl_or_b32 v2, v2, 6, v3
	s_lshl_b32 s4, s9, 4
	s_add_i32 s5, s28, s4
	s_lshl_b32 s5, s5, 6
	s_add_i32 s6, s29, s4
	s_lshl_b32 s6, s6, 6
	s_lshl_b32 s8, s9, 10
	s_waitcnt lgkmcnt(0)
	s_add_u32 s10, s0, s5
	s_addc_u32 s11, s1, 0
	s_add_u32 s12, s10, 0x1000
	s_addc_u32 s13, s11, 0
	s_add_u32 s14, s12, 0x1000
	s_addc_u32 s15, s13, 0
	s_add_u32 s16, s2, s6
	s_addc_u32 s17, s3, 0
	s_add_u32 s18, s16, 0x1000
	s_addc_u32 s19, s17, 0
	s_add_u32 s24, s18, 0x1000
	s_addc_u32 s25, s19, 0
	s_add_u32 s26, s24, 0x1000
	s_addc_u32 s27, s25, 0
	v_mov_b32_e32 v5, v2
	v_mov_b32_e32 v6, v2
	s_add_i32 m0, s8, 0
	s_nop 0
	global_load_lds_dwordx4 v5, s[10:11]
	s_add_i32 m0, s8, 4096
	s_nop 0
	global_load_lds_dwordx4 v5, s[12:13]
	s_add_i32 m0, s8, 8192
	s_nop 0
	global_load_lds_dwordx4 v5, s[14:15]
	s_add_i32 m0, s8, 12288
	s_nop 0
	global_load_lds_dwordx4 v6, s[16:17]
	s_add_i32 m0, s8, 16384
	s_nop 0
	global_load_lds_dwordx4 v6, s[18:19]
	s_add_i32 m0, s8, 20480
	s_nop 0
	global_load_lds_dwordx4 v6, s[24:25]
	s_add_i32 m0, s8, 24576
	s_nop 0
	global_load_lds_dwordx4 v6, s[26:27]
	v_add_u32_e32 v5, 196608, v5
	v_add_u32_e32 v6, 262144, v6
	s_add_i32 m0, s8, 28672
	s_nop 0
	global_load_lds_dwordx4 v5, s[10:11]
	s_add_i32 m0, s8, 32768
	s_nop 0
	global_load_lds_dwordx4 v5, s[12:13]
	s_add_i32 m0, s8, 36864
	s_nop 0
	global_load_lds_dwordx4 v5, s[14:15]
	s_add_i32 m0, s8, 40960
	s_nop 0
	global_load_lds_dwordx4 v6, s[16:17]
	s_add_i32 m0, s8, 45056
	s_nop 0
	global_load_lds_dwordx4 v6, s[18:19]
	s_add_i32 m0, s8, 49152
	s_nop 0
	global_load_lds_dwordx4 v6, s[24:25]
	s_add_i32 m0, s8, 53248
	s_nop 0
	global_load_lds_dwordx4 v6, s[26:27]
	v_add_u32_e32 v5, 196608, v5
	v_add_u32_e32 v6, 262144, v6
	s_add_i32 m0, s8, 57344
	s_nop 0
	global_load_lds_dwordx4 v5, s[10:11]
	s_add_i32 m0, s8, 61440
	s_nop 0
	global_load_lds_dwordx4 v5, s[12:13]
	s_add_i32 m0, s8, 65536
	s_nop 0
	global_load_lds_dwordx4 v5, s[14:15]
	s_add_i32 m0, s8, 69632
	s_nop 0
	global_load_lds_dwordx4 v6, s[16:17]
	s_add_i32 m0, s8, 73728
	s_nop 0
	global_load_lds_dwordx4 v6, s[18:19]
	s_add_i32 m0, s8, 77824
	s_nop 0
	global_load_lds_dwordx4 v6, s[24:25]
	s_add_i32 m0, s8, 81920
	s_nop 0
	global_load_lds_dwordx4 v6, s[26:27]
	v_add_u32_e32 v5, 196608, v5
	v_add_u32_e32 v6, 262144, v6
	s_add_i32 m0, s8, 86016
	s_nop 0
	global_load_lds_dwordx4 v5, s[10:11]
	s_add_i32 m0, s8, 90112
	s_nop 0
	global_load_lds_dwordx4 v5, s[12:13]
	s_add_i32 m0, s8, 94208
	s_nop 0
	global_load_lds_dwordx4 v5, s[14:15]
	s_add_i32 m0, s8, 98304
	s_nop 0
	global_load_lds_dwordx4 v6, s[16:17]
	s_add_i32 m0, s8, 102400
	s_nop 0
	global_load_lds_dwordx4 v6, s[18:19]
	s_add_i32 m0, s8, 106496
	s_nop 0
	global_load_lds_dwordx4 v6, s[24:25]
	s_add_i32 m0, s8, 110592
	s_nop 0
	global_load_lds_dwordx4 v6, s[26:27]
	v_add_u32_e32 v5, 196608, v5
	v_add_u32_e32 v6, 262144, v6
	s_waitcnt vmcnt(21)
	s_barrier
	s_mov_b32 s29, 4
	s_mov_b32 s30, 28
	.p2align	6

.LBB3_3:
	v_lshrrev_b32_e32 v2, 2, v0
	v_sub_u32_e32 v2, 0, v2
	s_lshr_b32 s9, s5, 2
	s_load_dwordx2 s[2:3], s[0:1], 0x30
	s_load_dwordx2 s[14:15], s[0:1], 0x8
	v_and_b32_e32 v34, 15, v0
	v_bitop3_b32 v2, v1, v2, 3 bitop3:0x78
	s_and_b32 s9, s9, 64
	s_lshl_b32 s10, s6, 5
	v_lshlrev_b32_e32 v35, 4, v2
	v_or_b32_e32 v2, s9, v34
	s_and_b32 s10, s10, 0x60
	v_lshlrev_b32_e32 v36, 6, v2
	v_or_b32_e32 v2, s10, v34
	v_lshlrev_b32_e32 v37, 6, v2
	v_mov_b32_e32 v2, 0
	s_mov_b32 s8, 0
	s_mov_b32 s11, 32
	v_mov_b32_e32 v3, v2
	v_mov_b32_e32 v4, v2
	v_mov_b32_e32 v5, v2
	v_mov_b32_e32 v10, v2
	v_mov_b32_e32 v11, v2
	v_mov_b32_e32 v12, v2
	v_mov_b32_e32 v13, v2
	v_mov_b32_e32 v6, v2
	v_mov_b32_e32 v7, v2
	v_mov_b32_e32 v8, v2
	v_mov_b32_e32 v9, v2
	v_mov_b32_e32 v18, v2
	v_mov_b32_e32 v19, v2
	v_mov_b32_e32 v20, v2
	v_mov_b32_e32 v21, v2
	v_mov_b32_e32 v14, v2
	v_mov_b32_e32 v15, v2
	v_mov_b32_e32 v16, v2
	v_mov_b32_e32 v17, v2
	v_mov_b32_e32 v26, v2
	v_mov_b32_e32 v27, v2
	v_mov_b32_e32 v28, v2
	v_mov_b32_e32 v29, v2
	v_mov_b32_e32 v22, v2
	v_mov_b32_e32 v23, v2
	v_mov_b32_e32 v24, v2
	v_mov_b32_e32 v25, v2
	v_mov_b32_e32 v30, v2
	v_mov_b32_e32 v31, v2
	v_mov_b32_e32 v32, v2
	v_mov_b32_e32 v33, v2
	v_and_b32_e32 v62, 63, v0
	v_lshrrev_b32_e32 v63, 2, v62
	v_and_b32_e32 v62, 3, v62
	v_sub_u32_e32 v64, 0, v1
	v_and_b32_e32 v64, 3, v64
	v_xor_b32_e32 v62, v62, v64
	v_lshlrev_b32_e32 v62, 4, v62
	v_lshl_or_b32 v62, v63, 11, v62
	s_lshl_b32 s13, s6, 4
	s_add_i32 s13, s13, s4
	s_lshl_b32 s13, s13, 11
	s_lshl_b32 s16, s6, 10
	s_add_i32 s16, s16, 0x2000
	s_waitcnt lgkmcnt(0)
	s_add_u32 s14, s14, s13
	s_addc_u32 s15, s15, 0
	s_add_i32 m0, s16, 0
	s_nop 0
	global_load_lds_dwordx4 v62, s[14:15] offset:0
	s_add_i32 m0, s16, 16320
	s_nop 0
	global_load_lds_dwordx4 v62, s[14:15] offset:64
	s_add_i32 m0, s16, 32640
	s_nop 0
	global_load_lds_dwordx4 v62, s[14:15] offset:128
	s_add_i32 m0, s16, 48960
	s_nop 0
	global_load_lds_dwordx4 v62, s[14:15] offset:192
	v_add_u32_e32 v62, 0x100, v62
	s_mov_b32 s17, 4
	.p2align	6

.LBB3_6:
	s_load_dwordx4 s[0:3], s[0:1], 0x0
	s_add_i32 s9, s6, -8
	s_mov_b32 s28, s7
	s_mov_b32 s29, s4
	v_and_b32_e32 v1, 63, v0
	v_bfe_u32 v3, v0, 4, 2
	v_lshrrev_b32_e32 v2, 2, v1
	v_sub_u32_e32 v3, 0, v3
	v_and_b32_e32 v3, 3, v3
	v_and_b32_e32 v4, 3, v1
	v_xor_b32_e32 v3, v3, v4
	v_lshlrev_b32_e32 v3, 4, v3
	v_lshl_or_b32 v2, v2, 11, v3
	s_lshl_b32 s4, s9, 4
	s_add_i32 s5, s28, s4
	s_lshl_b32 s5, s5, 11
	s_add_i32 s6, s29, s4
	s_lshl_b32 s6, s6, 11
	s_lshl_b32 s8, s9, 10
	s_waitcnt lgkmcnt(0)
	s_add_u32 s10, s0, s5
	s_addc_u32 s11, s1, 0
	s_add_u32 s12, s10, 131072
	s_addc_u32 s13, s11, 0
	v_mov_b32_e32 v5, v2
	v_mov_b32_e32 v6, v2
	s_add_i32 m0, s8, 0
	s_nop 0
	global_load_lds_dwordx4 v5, s[10:11]
	s_add_i32 m0, s8, 4096
	s_nop 0
	global_load_lds_dwordx4 v5, s[12:13]
	v_add_u32_e32 v5, 64, v5
	v_add_u32_e32 v6, 64, v6
	s_add_i32 m0, s8, 16384
	s_nop 0
	global_load_lds_dwordx4 v5, s[10:11]
	s_add_i32 m0, s8, 20480
	s_nop 0
	global_load_lds_dwordx4 v5, s[12:13]
	v_add_u32_e32 v5, 64, v5
	v_add_u32_e32 v6, 64, v6
	s_add_i32 m0, s8, 32768
	s_nop 0
	global_load_lds_dwordx4 v5, s[10:11]
	s_add_i32 m0, s8, 36864
	s_nop 0
	global_load_lds_dwordx4 v5, s[12:13]
	v_add_u32_e32 v5, 64, v5
	v_add_u32_e32 v6, 64, v6
	s_add_i32 m0, s8, 49152
	s_nop 0
	global_load_lds_dwordx4 v5, s[10:11]
	s_add_i32 m0, s8, 53248
	s_nop 0
	global_load_lds_dwordx4 v5, s[12:13]
	v_add_u32_e32 v5, 64, v5
	v_add_u32_e32 v6, 64, v6
	s_mov_b32 s29, 4
	s_mov_b32 s30, 28
	.p2align	6
